# speedup vs baseline: 1.0363x; 1.0042x over previous
.LBB1_3:
	s_mov_b32 s29, s16
	v_add_u32_e32 v0, s29, v101
	ds_read_b128 v[94:97], v0 offset:16384
	ds_read_b128 v[102:105], v0 offset:17408
	ds_read_b128 v[106:109], v0 offset:18432
	ds_read_b128 v[110:113], v0 offset:19456
	ds_read_b128 v[114:117], v0 offset:32768
	ds_read_b128 v[118:121], v0 offset:33792
	ds_read_b128 v[122:125], v0 offset:34816
	ds_read_b128 v[126:129], v0 offset:35840
	v_add_u32_e32 v0, s29, v91
	ds_read_b128 v[130:133], v0
	ds_read_b128 v[134:137], v0 offset:1024
	ds_read_b128 v[138:141], v0 offset:2048
	ds_read_b128 v[142:145], v0 offset:3072
	ds_read_b128 v[146:149], v0 offset:4096
	ds_read_b128 v[150:153], v0 offset:5120
	ds_read_b128 v[154:157], v0 offset:6144
	ds_read_b128 v[158:161], v0 offset:7168
	s_lshl_b32 s16, s28, 2
	s_or_b32 s16, s16, s23
	s_lshl_b64 s[30:31], s[16:17], 19
	s_add_u32 s16, s6, s30
	s_addc_u32 s31, s7, s31
	s_lshl_b32 s33, s3, 7
	s_ashr_i32 s35, s33, 31
	s_add_u32 s30, s16, s33
	s_addc_u32 s31, s31, s35
	s_add_u32 s34, s4, s33
	s_addc_u32 s35, s5, s35
	s_add_i32 s16, s19, s27
	s_add_i32 m0, s16, 0x4000
	s_nop 0
	global_load_lds_dwordx4 v84, s[30:31]
	s_add_i32 m0, s16, 0x6000
	s_nop 0
	global_load_lds_dwordx4 v88, s[30:31]
	s_mov_b32 m0, s16
	s_nop 0
	global_load_lds_dwordx4 v82, s[34:35]
	s_waitcnt vmcnt(3)
	s_waitcnt lgkmcnt(0)
	s_barrier
	s_setprio 1
	s_waitcnt lgkmcnt(0)
	v_mfma_f32_16x16x32_f16 v[78:81], v[94:97], v[130:133], v[78:81]
	v_mfma_f32_16x16x32_f16 v[74:77], v[106:109], v[130:133], v[74:77]
	v_mfma_f32_16x16x32_f16 v[66:69], v[94:97], v[138:141], v[66:69]
	v_mfma_f32_16x16x32_f16 v[58:61], v[106:109], v[138:141], v[58:61]
	v_mfma_f32_16x16x32_f16 v[78:81], v[102:105], v[134:137], v[78:81]
	s_add_u32 s30, s30, 0x40000
	v_mfma_f32_16x16x32_f16 v[74:77], v[110:113], v[134:137], v[74:77]
	s_addc_u32 s31, s31, 0
	s_add_i32 m0, s16, 0x8000
	v_mfma_f32_16x16x32_f16 v[66:69], v[102:105], v[142:145], v[66:69]
	v_mfma_f32_16x16x32_f16 v[58:61], v[110:113], v[142:145], v[58:61]
	global_load_lds_dwordx4 v84, s[30:31]
	v_mfma_f32_16x16x32_f16 v[54:57], v[94:97], v[146:149], v[54:57]
	v_mfma_f32_16x16x32_f16 v[46:49], v[106:109], v[146:149], v[46:49]
	v_mfma_f32_16x16x32_f16 v[34:37], v[94:97], v[154:157], v[34:37]
	v_mfma_f32_16x16x32_f16 v[26:29], v[106:109], v[154:157], v[26:29]
	v_mfma_f32_16x16x32_f16 v[54:57], v[102:105], v[150:153], v[54:57]
	v_mfma_f32_16x16x32_f16 v[46:49], v[110:113], v[150:153], v[46:49]
	s_add_i32 m0, s16, 0xa000
	v_mfma_f32_16x16x32_f16 v[34:37], v[102:105], v[158:161], v[34:37]
	v_mfma_f32_16x16x32_f16 v[26:29], v[110:113], v[158:161], v[26:29]
	global_load_lds_dwordx4 v88, s[30:31]
	v_mfma_f32_16x16x32_f16 v[70:73], v[114:117], v[130:133], v[70:73]
	v_mfma_f32_16x16x32_f16 v[62:65], v[122:125], v[130:133], v[62:65]
	v_mfma_f32_16x16x32_f16 v[50:53], v[114:117], v[138:141], v[50:53]
	v_mfma_f32_16x16x32_f16 v[42:45], v[122:125], v[138:141], v[42:45]
	v_mfma_f32_16x16x32_f16 v[70:73], v[118:121], v[134:137], v[70:73]
	v_mfma_f32_16x16x32_f16 v[62:65], v[126:129], v[134:137], v[62:65]
	s_add_i32 m0, s16, 0x2000
	v_mfma_f32_16x16x32_f16 v[50:53], v[118:121], v[142:145], v[50:53]
	v_mfma_f32_16x16x32_f16 v[42:45], v[126:129], v[142:145], v[42:45]
	global_load_lds_dwordx4 v86, s[34:35]
	v_mfma_f32_16x16x32_f16 v[38:41], v[114:117], v[146:149], v[38:41]
	v_mfma_f32_16x16x32_f16 v[30:33], v[122:125], v[146:149], v[30:33]
	s_add_i32 s3, s3, 1
	s_cmp_lt_u32 s28, 2
	s_cselect_b64 s[30:31], -1, 0
	v_mfma_f32_16x16x32_f16 v[22:25], v[114:117], v[154:157], v[22:25]
	s_cmp_eq_u32 s3, 16
	s_cselect_b64 s[34:35], -1, 0
	v_mfma_f32_16x16x32_f16 v[2:5], v[122:125], v[154:157], v[2:5]
	s_and_b64 s[36:37], s[34:35], exec
	s_cselect_b32 s3, 0, s3
	v_mfma_f32_16x16x32_f16 v[38:41], v[118:121], v[150:153], v[38:41]
	s_and_b64 s[30:31], s[34:35], s[30:31]
	s_cmp_lg_u64 s[30:31], 0
	v_mfma_f32_16x16x32_f16 v[30:33], v[126:129], v[150:153], v[30:33]
	s_addc_u32 s28, s28, 0
	s_add_i32 s26, s26, -1
	v_mfma_f32_16x16x32_f16 v[22:25], v[118:121], v[158:161], v[22:25]
	s_mov_b32 s16, s24
	s_mov_b32 s24, s27
	v_mfma_f32_16x16x32_f16 v[2:5], v[126:129], v[158:161], v[2:5]
	s_mov_b32 s27, s29
	s_cmp_lg_u32 s26, 0
	s_setprio 0
	s_barrier
	s_cbranch_scc1 .LBB1_3
	s_lshl_b32 s3, s14, 7
	s_add_i32 s17, s25, s3
	s_ashr_i32 s3, s17, 1
	s_lshr_b32 s14, s17, 5
	s_or_b32 s24, s15, s2
	s_and_b32 s14, s14, 62
	s_and_b32 s27, s3, 0xfffffc00
	v_or_b32_e32 v105, s24, v1
	v_lshlrev_b32_e32 v98, 4, v93
	v_or_b32_e32 v102, 16, v93
	v_or_b32_e32 v103, 32, v93
	v_or_b32_e32 v104, 48, v93
	v_mov_b32_e32 v93, 0
	s_and_b32 s16, s24, 0x340
	v_lshlrev_b32_e32 v95, 6, v105
	s_or_b32 s2, s27, s14
	v_lshlrev_b32_e32 v0, 9, v92
	v_and_b32_e32 v110, 0xc00, v95
	v_mov_b32_e32 v111, v93
	s_or_b32 s14, s2, s16
	v_and_b32_e32 v92, 0x200, v0
	v_lshl_add_u64 v[110:111], s[8:9], 0, v[110:111]
	s_or_b32 s30, s14, 0x80
	s_mov_b32 s3, 0
	v_mov_b32_e32 v99, v93
	v_lshl_add_u64 v[110:111], v[110:111], 0, v[92:93]
	s_mov_b32 s2, 0x3e38aa3b
	v_pk_add_f32 v[72:73], v[12:13], v[72:73]
	v_pk_add_f32 v[70:71], v[10:11], v[70:71]
	v_pk_add_f32 v[64:65], v[8:9], v[64:65]
	v_pk_add_f32 v[62:63], v[6:7], v[62:63]
	s_ashr_i32 s31, s30, 31
	v_lshl_add_u64 v[112:113], v[110:111], 0, v[98:99]
	v_pk_mul_f32 v[72:73], v[72:73], s[2:3] op_sel_hi:[1,0]
	v_pk_mul_f32 v[70:71], v[70:71], s[2:3] op_sel_hi:[1,0]
	v_pk_mul_f32 v[64:65], v[64:65], s[2:3] op_sel_hi:[1,0]
	v_pk_mul_f32 v[62:63], v[62:63], s[2:3] op_sel_hi:[1,0]
	s_lshl_b64 s[30:31], s[30:31], 12
	v_lshlrev_b32_e32 v96, 4, v102
	v_mov_b32_e32 v97, v93
	v_pk_add_f32 v[80:81], v[20:21], v[80:81]
	v_pk_add_f32 v[78:79], v[18:19], v[78:79]
	v_pk_add_f32 v[74:75], v[14:15], v[74:75]
	s_ashr_i32 s15, s14, 31
	v_cvt_pk_f16_f32 v70, v70, v71
	v_cvt_pk_f16_f32 v71, v72, v73
	v_cvt_pk_f16_f32 v72, v62, v63
	v_cvt_pk_f16_f32 v73, v64, v65
	v_lshl_add_u64 v[62:63], v[112:113], 0, s[30:31]
	v_pk_add_f32 v[58:59], v[14:15], v[58:59]
	v_pk_mul_f32 v[80:81], v[80:81], s[2:3] op_sel_hi:[1,0]
	v_pk_mul_f32 v[78:79], v[78:79], s[2:3] op_sel_hi:[1,0]
	v_pk_mul_f32 v[74:75], v[74:75], s[2:3] op_sel_hi:[1,0]
	s_lshl_b64 s[28:29], s[14:15], 12
	global_store_dwordx4 v[62:63], v[70:73], off sc1
	v_pk_add_f32 v[62:63], v[20:21], v[68:69]
	v_pk_add_f32 v[64:65], v[18:19], v[66:67]
	v_lshl_add_u64 v[70:71], v[110:111], 0, v[96:97]
	v_pk_mul_f32 v[58:59], v[58:59], s[2:3] op_sel_hi:[1,0]
	v_pk_add_f32 v[52:53], v[12:13], v[52:53]
	v_pk_add_f32 v[50:51], v[10:11], v[50:51]
	v_pk_add_f32 v[44:45], v[8:9], v[44:45]
	v_pk_add_f32 v[42:43], v[6:7], v[42:43]
	v_lshlrev_b32_e32 v0, 4, v103
	v_cvt_pk_f16_f32 v78, v78, v79
	v_cvt_pk_f16_f32 v79, v80, v81
	v_cvt_pk_f16_f32 v80, v74, v75
	v_lshl_add_u64 v[74:75], v[112:113], 0, s[28:29]
	v_pk_mul_f32 v[66:67], v[62:63], s[2:3] op_sel_hi:[1,0]
	v_pk_mul_f32 v[62:63], v[64:65], s[2:3] op_sel_hi:[1,0]
	v_cvt_pk_f16_f32 v64, v58, v59
	v_lshl_add_u64 v[58:59], v[70:71], 0, s[28:29]
	v_pk_mul_f32 v[52:53], v[52:53], s[2:3] op_sel_hi:[1,0]
	v_pk_mul_f32 v[50:51], v[50:51], s[2:3] op_sel_hi:[1,0]
	v_pk_mul_f32 v[44:45], v[44:45], s[2:3] op_sel_hi:[1,0]
	v_pk_mul_f32 v[42:43], v[42:43], s[2:3] op_sel_hi:[1,0]
	s_or_b32 s28, s14, 1
	s_or_b32 s14, s14, 0x81
	v_and_b32_e32 v106, 0xf0, v0
	v_mov_b32_e32 v107, v93
	v_cvt_pk_f16_f32 v50, v50, v51
	v_cvt_pk_f16_f32 v51, v52, v53
	v_cvt_pk_f16_f32 v52, v42, v43
	v_cvt_pk_f16_f32 v53, v44, v45
	v_lshl_add_u64 v[42:43], v[70:71], 0, s[30:31]
	v_pk_add_f32 v[40:41], v[12:13], v[40:41]
	v_pk_add_f32 v[38:39], v[10:11], v[38:39]
	v_pk_add_f32 v[32:33], v[8:9], v[32:33]
	v_pk_add_f32 v[30:31], v[6:7], v[30:31]
	s_ashr_i32 s15, s14, 31
	v_lshlrev_b32_e32 v94, 4, v104
	global_store_dwordx4 v[42:43], v[50:53], off sc1
	v_pk_mul_f32 v[40:41], v[40:41], s[2:3] op_sel_hi:[1,0]
	v_pk_mul_f32 v[38:39], v[38:39], s[2:3] op_sel_hi:[1,0]
	v_lshl_add_u64 v[50:51], v[110:111], 0, v[106:107]
	v_pk_mul_f32 v[32:33], v[32:33], s[2:3] op_sel_hi:[1,0]
	v_pk_mul_f32 v[30:31], v[30:31], s[2:3] op_sel_hi:[1,0]
	s_lshl_b64 s[14:15], s[14:15], 12
	v_and_b32_e32 v108, 0x1f0, v94
	v_mov_b32_e32 v109, v93
	v_pk_add_f32 v[42:43], v[20:21], v[56:57]
	v_pk_add_f32 v[44:45], v[18:19], v[54:55]
	v_pk_add_f32 v[46:47], v[14:15], v[46:47]
	s_ashr_i32 s29, s28, 31
	v_cvt_pk_f16_f32 v38, v38, v39
	v_cvt_pk_f16_f32 v39, v40, v41
	v_cvt_pk_f16_f32 v40, v30, v31
	v_cvt_pk_f16_f32 v41, v32, v33
	v_lshl_add_u64 v[30:31], v[50:51], 0, s[14:15]
	v_pk_add_f32 v[20:21], v[20:21], v[36:37]
	v_pk_add_f32 v[18:19], v[18:19], v[34:35]
	v_pk_add_f32 v[14:15], v[14:15], v[26:27]
	v_pk_add_f32 v[76:77], v[16:17], v[76:77]
	v_pk_add_f32 v[60:61], v[16:17], v[60:61]
	v_pk_mul_f32 v[52:53], v[42:43], s[2:3] op_sel_hi:[1,0]
	v_pk_mul_f32 v[42:43], v[44:45], s[2:3] op_sel_hi:[1,0]
	v_pk_add_f32 v[44:45], v[16:17], v[48:49]
	s_lshl_b64 s[28:29], s[28:29], 12
	global_store_dwordx4 v[30:31], v[38:41], off sc1
	v_lshl_add_u64 v[30:31], v[110:111], 0, v[108:109]
	v_pk_mul_f32 v[20:21], v[20:21], s[2:3] op_sel_hi:[1,0]
	v_pk_mul_f32 v[18:19], v[18:19], s[2:3] op_sel_hi:[1,0]
	v_pk_add_f32 v[16:17], v[16:17], v[28:29]
	v_pk_mul_f32 v[14:15], v[14:15], s[2:3] op_sel_hi:[1,0]
	v_pk_add_f32 v[12:13], v[12:13], v[24:25]
	v_pk_add_f32 v[10:11], v[10:11], v[22:23]
	v_pk_add_f32 v[4:5], v[8:9], v[4:5]
	v_pk_add_f32 v[2:3], v[6:7], v[2:3]
	v_pk_mul_f32 v[76:77], v[76:77], s[2:3] op_sel_hi:[1,0]
	v_pk_mul_f32 v[60:61], v[60:61], s[2:3] op_sel_hi:[1,0]
	v_pk_mul_f32 v[48:49], v[44:45], s[2:3] op_sel_hi:[1,0]
	v_pk_mul_f32 v[44:45], v[46:47], s[2:3] op_sel_hi:[1,0]
	v_lshl_add_u64 v[46:47], v[50:51], 0, s[28:29]
	v_cvt_pk_f16_f32 v18, v18, v19
	v_cvt_pk_f16_f32 v19, v20, v21
	v_pk_mul_f32 v[16:17], v[16:17], s[2:3] op_sel_hi:[1,0]
	v_cvt_pk_f16_f32 v20, v14, v15
	v_lshl_add_u64 v[14:15], v[30:31], 0, s[28:29]
	v_pk_mul_f32 v[12:13], v[12:13], s[2:3] op_sel_hi:[1,0]
	v_pk_mul_f32 v[10:11], v[10:11], s[2:3] op_sel_hi:[1,0]
	v_pk_mul_f32 v[4:5], v[4:5], s[2:3] op_sel_hi:[1,0]
	v_pk_mul_f32 v[2:3], v[2:3], s[2:3] op_sel_hi:[1,0]
	s_add_u32 s28, s20, s22
	v_cvt_pk_f16_f32 v81, v76, v77
	v_cvt_pk_f16_f32 v62, v62, v63
	v_cvt_pk_f16_f32 v63, v66, v67
	v_cvt_pk_f16_f32 v65, v60, v61
	v_cvt_pk_f16_f32 v42, v42, v43
	v_cvt_pk_f16_f32 v43, v52, v53
	v_cvt_pk_f16_f32 v44, v44, v45
	v_cvt_pk_f16_f32 v45, v48, v49
	v_cvt_pk_f16_f32 v21, v16, v17
	v_cvt_pk_f16_f32 v10, v10, v11
	v_cvt_pk_f16_f32 v11, v12, v13
	v_cvt_pk_f16_f32 v12, v2, v3
	v_cvt_pk_f16_f32 v13, v4, v5
	v_lshl_add_u64 v[2:3], v[30:31], 0, s[14:15]
	s_addc_u32 s29, s21, 0
	v_lshlrev_b32_e32 v92, 2, v1
	global_store_dwordx4 v[74:75], v[78:81], off sc1
	global_store_dwordx4 v[58:59], v[62:65], off sc1
	global_store_dwordx4 v[46:47], v[42:45], off sc1
	global_store_dwordx4 v[14:15], v[18:21], off sc1
	global_store_dwordx4 v[2:3], v[10:13], off sc1
	v_lshl_add_u64 v[2:3], s[28:29], 0, v[92:93]
	s_mov_b64 s[28:29], 0x1000
	v_lshl_add_u64 v[10:11], v[2:3], 0, s[28:29]
	global_load_dwordx4 v[22:25], v[10:11], off
	global_load_dwordx4 v[14:17], v[10:11], off offset:16
	global_load_dwordx4 v[6:9], v[10:11], off offset:512
	global_load_dwordx4 v[2:5], v[10:11], off offset:528
	s_mov_b32 s25, 1
	s_mov_b32 s26, 16
	s_mov_b32 s14, 2
	s_mov_b32 s15, 0x18000
	s_mov_b32 s2, 0xc000
	s_mov_b32 s27, 0
	v_mov_b32_e32 v10, v93
	v_mov_b32_e32 v11, v93
	v_mov_b32_e32 v12, v93
	v_mov_b32_e32 v13, v93
	v_mov_b32_e32 v18, v93
	v_mov_b32_e32 v19, v93
	v_mov_b32_e32 v20, v93
	v_mov_b32_e32 v21, v93
	v_mov_b32_e32 v26, v93
	v_mov_b32_e32 v27, v93
	v_mov_b32_e32 v28, v93
	v_mov_b32_e32 v29, v93
	v_mov_b32_e32 v34, v93
	v_mov_b32_e32 v35, v93
	v_mov_b32_e32 v36, v93
	v_mov_b32_e32 v37, v93
	v_mov_b32_e32 v42, v93
	v_mov_b32_e32 v43, v93
	v_mov_b32_e32 v44, v93
	v_mov_b32_e32 v45, v93
	v_mov_b32_e32 v50, v93
	v_mov_b32_e32 v51, v93
	v_mov_b32_e32 v52, v93
	v_mov_b32_e32 v53, v93
	v_mov_b32_e32 v62, v93
	v_mov_b32_e32 v63, v93
	v_mov_b32_e32 v64, v93
	v_mov_b32_e32 v65, v93
	v_mov_b32_e32 v70, v93
	v_mov_b32_e32 v71, v93
	v_mov_b32_e32 v72, v93
	v_mov_b32_e32 v73, v93
	v_mov_b32_e32 v30, v93
	v_mov_b32_e32 v31, v93
	v_mov_b32_e32 v32, v93
	v_mov_b32_e32 v33, v93
	v_mov_b32_e32 v38, v93
	v_mov_b32_e32 v39, v93
	v_mov_b32_e32 v40, v93
	v_mov_b32_e32 v41, v93
	v_mov_b32_e32 v46, v93
	v_mov_b32_e32 v47, v93
	v_mov_b32_e32 v48, v93
	v_mov_b32_e32 v49, v93
	v_mov_b32_e32 v54, v93
	v_mov_b32_e32 v55, v93
	v_mov_b32_e32 v56, v93
	v_mov_b32_e32 v57, v93
	v_mov_b32_e32 v58, v93
	v_mov_b32_e32 v59, v93
	v_mov_b32_e32 v60, v93
	v_mov_b32_e32 v61, v93
	v_mov_b32_e32 v66, v93
	v_mov_b32_e32 v67, v93
	v_mov_b32_e32 v68, v93
	v_mov_b32_e32 v69, v93
	v_mov_b32_e32 v74, v93
	v_mov_b32_e32 v75, v93
	v_mov_b32_e32 v76, v93
	v_mov_b32_e32 v77, v93
	v_mov_b32_e32 v78, v93
	v_mov_b32_e32 v79, v93
	v_mov_b32_e32 v80, v93
	v_mov_b32_e32 v81, v93
.LBB1_5:
	s_mov_b32 s28, s2
	v_add_u32_e32 v1, s28, v101
	ds_read_b128 v[106:109], v1 offset:16384
	ds_read_b128 v[110:113], v1 offset:17408
	ds_read_b128 v[114:117], v1 offset:18432
	ds_read_b128 v[118:121], v1 offset:19456
	ds_read_b128 v[122:125], v1 offset:32768
	ds_read_b128 v[126:129], v1 offset:33792
	ds_read_b128 v[130:133], v1 offset:34816
	ds_read_b128 v[134:137], v1 offset:35840
	v_add_u32_e32 v1, s28, v91
	ds_read_b128 v[138:141], v1
	ds_read_b128 v[142:145], v1 offset:1024
	ds_read_b128 v[146:149], v1 offset:2048
	ds_read_b128 v[150:153], v1 offset:3072
	ds_read_b128 v[154:157], v1 offset:4096
	ds_read_b128 v[158:161], v1 offset:5120
	ds_read_b128 v[162:165], v1 offset:6144
	ds_read_b128 v[166:169], v1 offset:7168
	s_lshl_b32 s2, s25, 2
	s_or_b32 s2, s2, s23
	s_lshl_b64 s[30:31], s[2:3], 19
	s_add_u32 s2, s6, s30
	s_addc_u32 s29, s7, s31
	s_lshl_b32 s33, s14, 7
	s_ashr_i32 s35, s33, 31
	s_add_u32 s30, s2, s33
	s_addc_u32 s31, s29, s35
	s_add_u32 s34, s4, s33
	s_addc_u32 s35, s5, s35
	s_add_i32 s2, s19, s27
	s_add_i32 m0, s2, 0x4000
	s_nop 0
	global_load_lds_dwordx4 v84, s[30:31]
	s_add_i32 m0, s2, 0x6000
	s_nop 0
	global_load_lds_dwordx4 v88, s[30:31]
	s_mov_b32 m0, s2
	s_nop 0
	global_load_lds_dwordx4 v82, s[34:35]
	s_waitcnt vmcnt(3)
	s_waitcnt lgkmcnt(0)
	s_barrier
	s_setprio 1
	s_waitcnt lgkmcnt(0)
	v_mfma_f32_16x16x32_f16 v[78:81], v[106:109], v[138:141], v[78:81]
	v_mfma_f32_16x16x32_f16 v[74:77], v[114:117], v[138:141], v[74:77]
	v_mfma_f32_16x16x32_f16 v[66:69], v[106:109], v[146:149], v[66:69]
	v_mfma_f32_16x16x32_f16 v[58:61], v[114:117], v[146:149], v[58:61]
	v_mfma_f32_16x16x32_f16 v[78:81], v[110:113], v[142:145], v[78:81]
	s_add_u32 s30, s30, 0x40000
	v_mfma_f32_16x16x32_f16 v[74:77], v[118:121], v[142:145], v[74:77]
	s_addc_u32 s31, s31, 0
	s_add_i32 m0, s2, 0x8000
	v_mfma_f32_16x16x32_f16 v[66:69], v[110:113], v[150:153], v[66:69]
	v_mfma_f32_16x16x32_f16 v[58:61], v[118:121], v[150:153], v[58:61]
	global_load_lds_dwordx4 v84, s[30:31]
	v_mfma_f32_16x16x32_f16 v[54:57], v[106:109], v[154:157], v[54:57]
	v_mfma_f32_16x16x32_f16 v[46:49], v[114:117], v[154:157], v[46:49]
	v_mfma_f32_16x16x32_f16 v[38:41], v[106:109], v[162:165], v[38:41]
	v_mfma_f32_16x16x32_f16 v[30:33], v[114:117], v[162:165], v[30:33]
	v_mfma_f32_16x16x32_f16 v[54:57], v[110:113], v[158:161], v[54:57]
	v_mfma_f32_16x16x32_f16 v[46:49], v[118:121], v[158:161], v[46:49]
	s_add_i32 m0, s2, 0xa000
	v_mfma_f32_16x16x32_f16 v[38:41], v[110:113], v[166:169], v[38:41]
	v_mfma_f32_16x16x32_f16 v[30:33], v[118:121], v[166:169], v[30:33]
	global_load_lds_dwordx4 v88, s[30:31]
	v_mfma_f32_16x16x32_f16 v[70:73], v[122:125], v[138:141], v[70:73]
	v_mfma_f32_16x16x32_f16 v[62:65], v[130:133], v[138:141], v[62:65]
	v_mfma_f32_16x16x32_f16 v[50:53], v[122:125], v[146:149], v[50:53]
	v_mfma_f32_16x16x32_f16 v[42:45], v[130:133], v[146:149], v[42:45]
	v_mfma_f32_16x16x32_f16 v[70:73], v[126:129], v[142:145], v[70:73]
	v_mfma_f32_16x16x32_f16 v[62:65], v[134:137], v[142:145], v[62:65]
	s_add_i32 m0, s2, 0x2000
	v_mfma_f32_16x16x32_f16 v[50:53], v[126:129], v[150:153], v[50:53]
	v_mfma_f32_16x16x32_f16 v[42:45], v[134:137], v[150:153], v[42:45]
	global_load_lds_dwordx4 v86, s[34:35]
	v_mfma_f32_16x16x32_f16 v[34:37], v[122:125], v[154:157], v[34:37]
	v_mfma_f32_16x16x32_f16 v[26:29], v[130:133], v[154:157], v[26:29]
	s_add_i32 s2, s14, 1
	s_cmp_lt_u32 s25, 2
	s_cselect_b64 s[30:31], -1, 0
	v_mfma_f32_16x16x32_f16 v[18:21], v[122:125], v[162:165], v[18:21]
	s_cmp_eq_u32 s2, 16
	s_cselect_b64 s[34:35], -1, 0
	v_mfma_f32_16x16x32_f16 v[10:13], v[130:133], v[162:165], v[10:13]
	s_and_b64 s[36:37], s[34:35], exec
	s_cselect_b32 s14, 0, s2
	v_mfma_f32_16x16x32_f16 v[34:37], v[126:129], v[158:161], v[34:37]
	s_and_b64 s[30:31], s[34:35], s[30:31]
	s_cmp_lg_u64 s[30:31], 0
	v_mfma_f32_16x16x32_f16 v[26:29], v[134:137], v[158:161], v[26:29]
	s_addc_u32 s25, s25, 0
	s_add_i32 s26, s26, -1
	v_mfma_f32_16x16x32_f16 v[18:21], v[126:129], v[166:169], v[18:21]
	s_mov_b32 s2, s15
	s_mov_b32 s15, s27
	v_mfma_f32_16x16x32_f16 v[10:13], v[134:137], v[166:169], v[10:13]
	s_mov_b32 s27, s28
	s_cmp_lg_u32 s26, 0
	s_setprio 0
	s_barrier
	s_cbranch_scc1 .LBB1_5
	s_ashr_i32 s2, s17, 7
	s_and_b32 s3, s2, -16
	s_or_b32 s2, s3, 2
	s_sub_u32 s14, s10, s8
	s_subb_u32 s11, s11, s9
	s_bfe_u32 s6, s17, 0x50006
	s_add_u32 s14, s8, s14
	s_addc_u32 s15, s9, s11
	s_lshr_b32 s11, s24, 6
	s_or_b32 s17, s11, s3
	s_lshl_b32 s17, s17, 8
	s_lshl_b32 s23, s6, 3
	v_bfe_u32 v93, v105, 3, 3
	v_pk_add_f32 v[80:81], v[24:25], v[80:81]
	v_pk_add_f32 v[78:79], v[22:23], v[78:79]
	v_pk_add_f32 v[74:75], v[14:15], v[74:75]
	s_or_b32 s17, s17, s23
	s_or_b32 s11, s2, s11
	v_cvt_pk_f16_f32 v78, v78, v79
	v_cvt_pk_f16_f32 v79, v80, v81
	v_cvt_pk_f16_f32 v80, v74, v75
	v_or_b32_e32 v74, s17, v93
	s_lshl_b32 s11, s11, 8
	v_ashrrev_i32_e32 v75, 31, v74
	v_pk_add_f32 v[72:73], v[8:9], v[72:73]
	v_pk_add_f32 v[70:71], v[6:7], v[70:71]
	v_pk_add_f32 v[62:63], v[2:3], v[62:63]
	s_or_b32 s11, s11, s23
	v_lshlrev_b64 v[74:75], 10, v[74:75]
	v_cvt_pk_f16_f32 v70, v70, v71
	v_cvt_pk_f16_f32 v71, v72, v73
	v_cvt_pk_f16_f32 v72, v62, v63
	v_or_b32_e32 v62, s11, v93
	v_pk_add_f32 v[76:77], v[16:17], v[76:77]
	v_lshl_add_u64 v[74:75], s[14:15], 0, v[74:75]
	v_ashrrev_i32_e32 v63, 31, v62
	v_cvt_pk_f16_f32 v81, v76, v77
	v_lshl_add_u64 v[76:77], v[74:75], 0, v[98:99]
	v_lshlrev_b64 v[62:63], 10, v[62:63]
	global_store_dwordx4 v[76:77], v[78:81], off sc1
	v_pk_add_f32 v[64:65], v[4:5], v[64:65]
	v_lshl_add_u64 v[76:77], s[14:15], 0, v[62:63]
	v_cvt_pk_f16_f32 v73, v64, v65
	v_lshl_add_u64 v[62:63], v[76:77], 0, v[98:99]
	global_store_dwordx4 v[62:63], v[70:73], off sc1
	v_pk_add_f32 v[64:65], v[24:25], v[68:69]
	v_pk_add_f32 v[62:63], v[22:23], v[66:67]
	v_pk_add_f32 v[60:61], v[16:17], v[60:61]
	v_pk_add_f32 v[58:59], v[14:15], v[58:59]
	v_pk_add_f32 v[52:53], v[8:9], v[52:53]
	v_pk_add_f32 v[50:51], v[6:7], v[50:51]
	v_pk_add_f32 v[44:45], v[4:5], v[44:45]
	v_pk_add_f32 v[42:43], v[2:3], v[42:43]
	v_cvt_pk_f16_f32 v62, v62, v63
	v_cvt_pk_f16_f32 v63, v64, v65
	v_cvt_pk_f16_f32 v64, v58, v59
	v_cvt_pk_f16_f32 v65, v60, v61
	v_lshl_add_u64 v[58:59], v[74:75], 0, v[96:97]
	v_cvt_pk_f16_f32 v50, v50, v51
	v_cvt_pk_f16_f32 v51, v52, v53
	v_cvt_pk_f16_f32 v52, v42, v43
	v_cvt_pk_f16_f32 v53, v44, v45
	v_lshl_add_u64 v[42:43], v[76:77], 0, v[96:97]
	v_mov_b32_e32 v1, 0
	global_store_dwordx4 v[58:59], v[62:65], off sc1
	global_store_dwordx4 v[42:43], v[50:53], off sc1
	v_pk_add_f32 v[44:45], v[24:25], v[56:57]
	v_pk_add_f32 v[42:43], v[22:23], v[54:55]
	v_mov_b32_e32 v95, v1
	v_cvt_pk_f16_f32 v42, v42, v43
	v_cvt_pk_f16_f32 v43, v44, v45
	v_pk_add_f32 v[48:49], v[16:17], v[48:49]
	v_pk_add_f32 v[44:45], v[14:15], v[46:47]
	v_pk_add_f32 v[36:37], v[8:9], v[36:37]
	v_pk_add_f32 v[34:35], v[6:7], v[34:35]
	v_pk_add_f32 v[28:29], v[4:5], v[28:29]
	v_pk_add_f32 v[26:27], v[2:3], v[26:27]
	v_pk_add_f32 v[24:25], v[24:25], v[40:41]
	v_pk_add_f32 v[22:23], v[22:23], v[38:39]
	v_pk_add_f32 v[16:17], v[16:17], v[32:33]
	v_pk_add_f32 v[14:15], v[14:15], v[30:31]
	v_pk_add_f32 v[8:9], v[8:9], v[20:21]
	v_pk_add_f32 v[6:7], v[6:7], v[18:19]
	v_pk_add_f32 v[4:5], v[4:5], v[12:13]
	v_pk_add_f32 v[2:3], v[2:3], v[10:11]
	s_add_u32 s14, s20, s22
	v_cvt_pk_f16_f32 v44, v44, v45
	v_cvt_pk_f16_f32 v45, v48, v49
	v_lshl_add_u64 v[46:47], v[74:75], 0, v[0:1]
	v_cvt_pk_f16_f32 v34, v34, v35
	v_cvt_pk_f16_f32 v35, v36, v37
	v_cvt_pk_f16_f32 v36, v26, v27
	v_cvt_pk_f16_f32 v37, v28, v29
	v_lshl_add_u64 v[26:27], v[76:77], 0, v[0:1]
	v_cvt_pk_f16_f32 v22, v22, v23
	v_cvt_pk_f16_f32 v23, v24, v25
	v_cvt_pk_f16_f32 v24, v14, v15
	v_cvt_pk_f16_f32 v25, v16, v17
	v_lshl_add_u64 v[14:15], v[74:75], 0, v[94:95]
	v_cvt_pk_f16_f32 v6, v6, v7
	v_cvt_pk_f16_f32 v7, v8, v9
	v_cvt_pk_f16_f32 v8, v2, v3
	v_cvt_pk_f16_f32 v9, v4, v5
	v_lshl_add_u64 v[2:3], v[76:77], 0, v[94:95]
	s_addc_u32 s15, s21, 0
	v_mov_b32_e32 v93, v1
	global_store_dwordx4 v[46:47], v[42:45], off sc1
	global_store_dwordx4 v[26:27], v[34:37], off sc1
	global_store_dwordx4 v[14:15], v[22:25], off sc1
	global_store_dwordx4 v[2:3], v[6:9], off sc1
	v_lshl_add_u64 v[2:3], s[14:15], 0, v[92:93]
	s_mov_b64 s[14:15], 0x2000
	v_lshl_add_u64 v[2:3], v[2:3], 0, s[14:15]
	global_load_dwordx4 v[20:23], v[2:3], off
	global_load_dwordx4 v[12:15], v[2:3], off offset:16
	global_load_dwordx4 v[8:11], v[2:3], off offset:512
	global_load_dwordx4 v[4:7], v[2:3], off offset:528
	s_add_u32 s11, s12, 0x400000
	s_mov_b32 s7, 2
	v_and_b32_e32 v106, 56, v105
	s_mov_b32 s10, 0
	s_addc_u32 s12, s13, 0
	s_mov_b32 s14, 0xc000
	s_mov_b32 s17, 0x18000
	s_mov_b32 s13, 16
	v_mov_b32_e32 v0, v1
	v_mov_b32_e32 v2, v1
	v_mov_b32_e32 v3, v1
	v_mov_b32_e32 v16, v1
	v_mov_b32_e32 v17, v1
	v_mov_b32_e32 v18, v1
	v_mov_b32_e32 v19, v1
	v_mov_b32_e32 v24, v1
	v_mov_b32_e32 v25, v1
	v_mov_b32_e32 v26, v1
	v_mov_b32_e32 v27, v1
	v_mov_b32_e32 v32, v1
	v_mov_b32_e32 v33, v1
	v_mov_b32_e32 v34, v1
	v_mov_b32_e32 v35, v1
	v_mov_b32_e32 v40, v1
	v_mov_b32_e32 v41, v1
	v_mov_b32_e32 v42, v1
	v_mov_b32_e32 v43, v1
	v_mov_b32_e32 v48, v1
	v_mov_b32_e32 v49, v1
	v_mov_b32_e32 v50, v1
	v_mov_b32_e32 v51, v1
	v_mov_b32_e32 v60, v1
	v_mov_b32_e32 v61, v1
	v_mov_b32_e32 v62, v1
	v_mov_b32_e32 v63, v1
	v_mov_b32_e32 v68, v1
	v_mov_b32_e32 v69, v1
	v_mov_b32_e32 v70, v1
	v_mov_b32_e32 v71, v1
	v_mov_b32_e32 v28, v1
	v_mov_b32_e32 v29, v1
	v_mov_b32_e32 v30, v1
	v_mov_b32_e32 v31, v1
	v_mov_b32_e32 v36, v1
	v_mov_b32_e32 v37, v1
	v_mov_b32_e32 v38, v1
	v_mov_b32_e32 v39, v1
	v_mov_b32_e32 v44, v1
	v_mov_b32_e32 v45, v1
	v_mov_b32_e32 v46, v1
	v_mov_b32_e32 v47, v1
	v_mov_b32_e32 v52, v1
	v_mov_b32_e32 v53, v1
	v_mov_b32_e32 v54, v1
	v_mov_b32_e32 v55, v1
	v_mov_b32_e32 v56, v1
	v_mov_b32_e32 v57, v1
	v_mov_b32_e32 v58, v1
	v_mov_b32_e32 v59, v1
	v_mov_b32_e32 v64, v1
	v_mov_b32_e32 v65, v1
	v_mov_b32_e32 v66, v1
	v_mov_b32_e32 v67, v1
	v_mov_b32_e32 v72, v1
	v_mov_b32_e32 v73, v1
	v_mov_b32_e32 v74, v1
	v_mov_b32_e32 v75, v1
	v_mov_b32_e32 v76, v1
	v_mov_b32_e32 v77, v1
	v_mov_b32_e32 v78, v1
	v_mov_b32_e32 v79, v1
.LBB1_7:
	s_mov_b32 s15, s17
	v_add_u32_e32 v80, s15, v101
	ds_read_b128 v[92:95], v80 offset:16384
	ds_read_b128 v[96:99], v80 offset:17408
	ds_read_b128 v[108:111], v80 offset:18432
	ds_read_b128 v[112:115], v80 offset:19456
	ds_read_b128 v[116:119], v80 offset:32768
	ds_read_b128 v[120:123], v80 offset:33792
	ds_read_b128 v[124:127], v80 offset:34816
	ds_read_b128 v[128:131], v80 offset:35840
	v_add_u32_e32 v80, s15, v91
	ds_read_b128 v[132:135], v80
	ds_read_b128 v[136:139], v80 offset:1024
	ds_read_b128 v[140:143], v80 offset:2048
	ds_read_b128 v[144:147], v80 offset:3072
	ds_read_b128 v[148:151], v80 offset:4096
	ds_read_b128 v[152:155], v80 offset:5120
	ds_read_b128 v[156:159], v80 offset:6144
	ds_read_b128 v[160:163], v80 offset:7168
	s_lshl_b32 s17, s7, 7
	s_ashr_i32 s23, s17, 31
	s_add_u32 s20, s11, s17
	s_addc_u32 s21, s12, s23
	s_add_u32 s22, s4, s17
	s_addc_u32 s23, s5, s23
	s_add_i32 s17, s19, s14
	s_add_i32 m0, s17, 0x4000
	s_nop 0
	global_load_lds_dwordx4 v84, s[20:21]
	s_add_i32 m0, s17, 0x6000
	s_nop 0
	global_load_lds_dwordx4 v88, s[20:21]
	s_mov_b32 m0, s17
	s_nop 0
	global_load_lds_dwordx4 v82, s[22:23]
	s_waitcnt vmcnt(3)
	s_waitcnt lgkmcnt(0)
	s_barrier
	s_setprio 1
	s_waitcnt lgkmcnt(0)
	v_mfma_f32_16x16x32_f16 v[76:79], v[92:95], v[132:135], v[76:79]
	v_mfma_f32_16x16x32_f16 v[72:75], v[108:111], v[132:135], v[72:75]
	v_mfma_f32_16x16x32_f16 v[64:67], v[92:95], v[140:143], v[64:67]
	v_mfma_f32_16x16x32_f16 v[56:59], v[108:111], v[140:143], v[56:59]
	v_mfma_f32_16x16x32_f16 v[76:79], v[96:99], v[136:139], v[76:79]
	s_add_u32 s20, s20, 0x40000
	v_mfma_f32_16x16x32_f16 v[72:75], v[112:115], v[136:139], v[72:75]
	s_addc_u32 s21, s21, 0
	s_add_i32 m0, s17, 0x8000
	v_mfma_f32_16x16x32_f16 v[64:67], v[96:99], v[144:147], v[64:67]
	v_mfma_f32_16x16x32_f16 v[56:59], v[112:115], v[144:147], v[56:59]
	global_load_lds_dwordx4 v84, s[20:21]
	v_mfma_f32_16x16x32_f16 v[52:55], v[92:95], v[148:151], v[52:55]
	v_mfma_f32_16x16x32_f16 v[44:47], v[108:111], v[148:151], v[44:47]
	v_mfma_f32_16x16x32_f16 v[36:39], v[92:95], v[156:159], v[36:39]
	v_mfma_f32_16x16x32_f16 v[28:31], v[108:111], v[156:159], v[28:31]
	v_mfma_f32_16x16x32_f16 v[52:55], v[96:99], v[152:155], v[52:55]
	v_mfma_f32_16x16x32_f16 v[44:47], v[112:115], v[152:155], v[44:47]
	s_add_i32 m0, s17, 0xa000
	v_mfma_f32_16x16x32_f16 v[36:39], v[96:99], v[160:163], v[36:39]
	v_mfma_f32_16x16x32_f16 v[28:31], v[112:115], v[160:163], v[28:31]
	global_load_lds_dwordx4 v88, s[20:21]
	v_mfma_f32_16x16x32_f16 v[68:71], v[116:119], v[132:135], v[68:71]
	v_mfma_f32_16x16x32_f16 v[60:63], v[124:127], v[132:135], v[60:63]
	v_mfma_f32_16x16x32_f16 v[48:51], v[116:119], v[140:143], v[48:51]
	v_mfma_f32_16x16x32_f16 v[40:43], v[124:127], v[140:143], v[40:43]
	v_mfma_f32_16x16x32_f16 v[68:71], v[120:123], v[136:139], v[68:71]
	v_mfma_f32_16x16x32_f16 v[60:63], v[128:131], v[136:139], v[60:63]
	s_add_i32 m0, s17, 0x2000
	v_mfma_f32_16x16x32_f16 v[48:51], v[120:123], v[144:147], v[48:51]
	v_mfma_f32_16x16x32_f16 v[40:43], v[128:131], v[144:147], v[40:43]
	global_load_lds_dwordx4 v86, s[22:23]
	v_mfma_f32_16x16x32_f16 v[32:35], v[116:119], v[148:151], v[32:35]
	v_mfma_f32_16x16x32_f16 v[24:27], v[124:127], v[148:151], v[24:27]
	s_add_i32 s7, s7, 1
	s_cmp_lg_u32 s7, 16
	v_mfma_f32_16x16x32_f16 v[16:19], v[116:119], v[156:159], v[16:19]
	s_cselect_b32 s7, s7, 0
	v_mfma_f32_16x16x32_f16 v[0:3], v[124:127], v[156:159], v[0:3]
	s_add_i32 s13, s13, -1
	v_mfma_f32_16x16x32_f16 v[32:35], v[120:123], v[152:155], v[32:35]
	s_mov_b32 s17, s10
	v_mfma_f32_16x16x32_f16 v[24:27], v[128:131], v[152:155], v[24:27]
	s_mov_b32 s10, s14
	v_mfma_f32_16x16x32_f16 v[16:19], v[120:123], v[160:163], v[16:19]
	s_mov_b32 s14, s15
	v_mfma_f32_16x16x32_f16 v[0:3], v[128:131], v[160:163], v[0:3]
	s_cmp_lg_u32 s13, 0
	s_setprio 0
	s_barrier
	s_cbranch_scc1 .LBB1_7
	s_sub_u32 s0, s0, s8
	s_subb_u32 s1, s1, s9
	s_add_u32 s0, s8, s0
	s_addc_u32 s1, s9, s1
	s_lshl_b32 s3, s3, 6
	s_or_b32 s3, s3, s16
	s_lshl_b32 s4, s6, 1
	v_lshrrev_b32_e32 v86, 5, v106
	v_pk_add_f32 v[78:79], v[22:23], v[78:79]
	v_pk_add_f32 v[76:77], v[20:21], v[76:77]
	v_pk_add_f32 v[72:73], v[12:13], v[72:73]
	s_or_b32 s3, s3, s4
	s_lshl_b32 s2, s2, 6
	v_cvt_pk_f16_f32 v76, v76, v77
	v_cvt_pk_f16_f32 v77, v78, v79
	v_cvt_pk_f16_f32 v78, v72, v73
	v_or_b32_e32 v72, s3, v86
	s_or_b32 s2, s2, s16
	v_ashrrev_i32_e32 v73, 31, v72
	v_pk_add_f32 v[70:71], v[10:11], v[70:71]
	v_pk_add_f32 v[68:69], v[8:9], v[68:69]
	v_pk_add_f32 v[60:61], v[4:5], v[60:61]
	s_or_b32 s2, s2, s4
	v_lshlrev_b64 v[72:73], 12, v[72:73]
	v_cvt_pk_f16_f32 v68, v68, v69
	v_cvt_pk_f16_f32 v69, v70, v71
	v_cvt_pk_f16_f32 v70, v60, v61
	v_or_b32_e32 v60, s2, v86
	v_mov_b32_e32 v91, 0
	v_pk_add_f32 v[74:75], v[14:15], v[74:75]
	v_lshl_add_u64 v[72:73], s[0:1], 0, v[72:73]
	v_ashrrev_i32_e32 v61, 31, v60
	v_cvt_pk_f16_f32 v79, v74, v75
	v_lshl_add_u64 v[74:75], v[72:73], 0, v[90:91]
	v_lshlrev_b64 v[60:61], 12, v[60:61]
	v_lshl_or_b32 v84, v102, 6, v100
	v_mov_b32_e32 v85, v91
	global_store_dwordx4 v[74:75], v[76:79], off sc1
	v_lshl_add_u64 v[74:75], s[0:1], 0, v[60:61]
	v_pk_add_f32 v[50:51], v[10:11], v[50:51]
	v_pk_add_f32 v[48:49], v[8:9], v[48:49]
	v_pk_add_f32 v[42:43], v[6:7], v[42:43]
	v_pk_add_f32 v[40:41], v[4:5], v[40:41]
	v_pk_add_f32 v[62:63], v[6:7], v[62:63]
	v_cvt_pk_f16_f32 v48, v48, v49
	v_cvt_pk_f16_f32 v49, v50, v51
	v_cvt_pk_f16_f32 v50, v40, v41
	v_cvt_pk_f16_f32 v51, v42, v43
	v_lshl_add_u64 v[40:41], v[74:75], 0, v[84:85]
	v_cvt_pk_f16_f32 v71, v62, v63
	v_lshl_add_u64 v[60:61], v[74:75], 0, v[90:91]
	global_store_dwordx4 v[40:41], v[48:51], off sc1
	v_pk_add_f32 v[42:43], v[22:23], v[54:55]
	v_pk_add_f32 v[40:41], v[20:21], v[52:53]
	v_lshl_or_b32 v80, v103, 6, v100
	v_lshl_or_b32 v82, v104, 6, v100
	v_mov_b32_e32 v81, v91
	v_mov_b32_e32 v83, v91
	global_store_dwordx4 v[60:61], v[68:71], off sc1
	v_pk_add_f32 v[62:63], v[22:23], v[66:67]
	v_pk_add_f32 v[60:61], v[20:21], v[64:65]
	v_pk_add_f32 v[58:59], v[14:15], v[58:59]
	v_pk_add_f32 v[56:57], v[12:13], v[56:57]
	v_cvt_pk_f16_f32 v40, v40, v41
	v_cvt_pk_f16_f32 v41, v42, v43
	v_pk_add_f32 v[46:47], v[14:15], v[46:47]
	v_pk_add_f32 v[42:43], v[12:13], v[44:45]
	v_pk_add_f32 v[34:35], v[10:11], v[34:35]
	v_pk_add_f32 v[32:33], v[8:9], v[32:33]
	v_pk_add_f32 v[26:27], v[6:7], v[26:27]
	v_pk_add_f32 v[24:25], v[4:5], v[24:25]
	v_pk_add_f32 v[22:23], v[22:23], v[38:39]
	v_pk_add_f32 v[20:21], v[20:21], v[36:37]
	v_pk_add_f32 v[14:15], v[14:15], v[30:31]
	v_pk_add_f32 v[12:13], v[12:13], v[28:29]
	v_pk_add_f32 v[10:11], v[10:11], v[18:19]
	v_pk_add_f32 v[8:9], v[8:9], v[16:17]
	v_pk_add_f32 v[2:3], v[6:7], v[2:3]
	v_pk_add_f32 v[0:1], v[4:5], v[0:1]
	v_cvt_pk_f16_f32 v60, v60, v61
	v_cvt_pk_f16_f32 v61, v62, v63
	v_cvt_pk_f16_f32 v62, v56, v57
	v_cvt_pk_f16_f32 v63, v58, v59
	v_lshl_add_u64 v[56:57], v[72:73], 0, v[84:85]
	v_cvt_pk_f16_f32 v42, v42, v43
	v_cvt_pk_f16_f32 v43, v46, v47
	v_lshl_add_u64 v[44:45], v[72:73], 0, v[80:81]
	v_cvt_pk_f16_f32 v32, v32, v33
	v_cvt_pk_f16_f32 v33, v34, v35
	v_cvt_pk_f16_f32 v34, v24, v25
	v_cvt_pk_f16_f32 v35, v26, v27
	v_lshl_add_u64 v[24:25], v[74:75], 0, v[80:81]
	v_cvt_pk_f16_f32 v20, v20, v21
	v_cvt_pk_f16_f32 v21, v22, v23
	v_cvt_pk_f16_f32 v22, v12, v13
	v_cvt_pk_f16_f32 v23, v14, v15
	v_lshl_add_u64 v[12:13], v[72:73], 0, v[82:83]
	v_cvt_pk_f16_f32 v8, v8, v9
	v_cvt_pk_f16_f32 v9, v10, v11
	v_cvt_pk_f16_f32 v10, v0, v1
	v_cvt_pk_f16_f32 v11, v2, v3
	v_lshl_add_u64 v[0:1], v[74:75], 0, v[82:83]
	global_store_dwordx4 v[56:57], v[60:63], off sc1
	global_store_dwordx4 v[44:45], v[40:43], off sc1
	global_store_dwordx4 v[24:25], v[32:35], off sc1
	global_store_dwordx4 v[12:13], v[20:23], off sc1
	global_store_dwordx4 v[0:1], v[8:11], off sc1
	s_waitcnt vmcnt(0)
	s_cmpk_gt_u32 s18, 0xff
	s_cbranch_scc1 .LBB1_10
	s_barrier

.LBB2_3:
	s_mov_b32 s16, s15
	v_add_u32_e32 v116, s16, v87
	v_add_u32_e32 v148, s16, v0
	ds_read_b128 v[88:91], v116 offset:16384
	ds_read_b128 v[92:95], v116 offset:17408
	ds_read_b128 v[96:99], v116 offset:18432
	ds_read_b128 v[100:103], v116 offset:19456
	ds_read_b128 v[104:107], v116 offset:32768
	ds_read_b128 v[108:111], v116 offset:33792
	ds_read_b128 v[112:115], v116 offset:34816
	ds_read_b128 v[116:119], v116 offset:35840
	ds_read_b128 v[120:123], v148
	ds_read_b128 v[124:127], v148 offset:1024
	ds_read_b128 v[128:131], v148 offset:2048
	ds_read_b128 v[132:135], v148 offset:3072
	ds_read_b128 v[136:139], v148 offset:4096
	ds_read_b128 v[140:143], v148 offset:5120
	ds_read_b128 v[144:147], v148 offset:6144
	ds_read_b128 v[148:151], v148 offset:7168
	s_lshl_b32 s15, s7, 7
	s_ashr_i32 s17, s15, 31
	s_add_u32 s18, s4, s15
	s_addc_u32 s19, s5, s17
	s_add_u32 s20, s2, s15
	s_addc_u32 s21, s3, s17
	s_add_i32 s15, s6, s14
	s_add_i32 m0, s15, 0x4000
	s_nop 0
	global_load_lds_dwordx4 v82, s[18:19]
	s_add_i32 m0, s15, 0x6000
	s_nop 0
	global_load_lds_dwordx4 v84, s[18:19]
	s_mov_b32 m0, s15
	s_nop 0
	global_load_lds_dwordx4 v82, s[20:21]
	s_waitcnt vmcnt(3)
	s_waitcnt lgkmcnt(0)
	s_barrier
	s_setprio 1
	s_waitcnt lgkmcnt(0)
	v_mfma_f32_16x16x32_f16 v[18:21], v[88:91], v[120:123], v[18:21]
	v_mfma_f32_16x16x32_f16 v[70:73], v[96:99], v[120:123], v[70:73]
	v_mfma_f32_16x16x32_f16 v[58:61], v[88:91], v[128:131], v[58:61]
	v_mfma_f32_16x16x32_f16 v[54:57], v[96:99], v[128:131], v[54:57]
	v_mfma_f32_16x16x32_f16 v[18:21], v[92:95], v[124:127], v[18:21]
	s_add_u32 s18, s18, 0x40000
	v_mfma_f32_16x16x32_f16 v[70:73], v[100:103], v[124:127], v[70:73]
	s_addc_u32 s19, s19, 0
	s_add_i32 m0, s15, 0x8000
	v_mfma_f32_16x16x32_f16 v[58:61], v[92:95], v[132:135], v[58:61]
	v_mfma_f32_16x16x32_f16 v[54:57], v[100:103], v[132:135], v[54:57]
	global_load_lds_dwordx4 v82, s[18:19]
	v_mfma_f32_16x16x32_f16 v[42:45], v[88:91], v[136:139], v[42:45]
	v_mfma_f32_16x16x32_f16 v[38:41], v[96:99], v[136:139], v[38:41]
	v_mfma_f32_16x16x32_f16 v[26:29], v[88:91], v[144:147], v[26:29]
	v_mfma_f32_16x16x32_f16 v[22:25], v[96:99], v[144:147], v[22:25]
	v_mfma_f32_16x16x32_f16 v[42:45], v[92:95], v[140:143], v[42:45]
	v_mfma_f32_16x16x32_f16 v[38:41], v[100:103], v[140:143], v[38:41]
	s_add_i32 m0, s15, 0xa000
	v_mfma_f32_16x16x32_f16 v[26:29], v[92:95], v[148:151], v[26:29]
	v_mfma_f32_16x16x32_f16 v[22:25], v[100:103], v[148:151], v[22:25]
	global_load_lds_dwordx4 v84, s[18:19]
	v_mfma_f32_16x16x32_f16 v[78:81], v[104:107], v[120:123], v[78:81]
	v_mfma_f32_16x16x32_f16 v[74:77], v[112:115], v[120:123], v[74:77]
	v_mfma_f32_16x16x32_f16 v[66:69], v[104:107], v[128:131], v[66:69]
	v_mfma_f32_16x16x32_f16 v[62:65], v[112:115], v[128:131], v[62:65]
	v_mfma_f32_16x16x32_f16 v[78:81], v[108:111], v[124:127], v[78:81]
	v_mfma_f32_16x16x32_f16 v[74:77], v[116:119], v[124:127], v[74:77]
	s_add_i32 m0, s15, 0x2000
	v_mfma_f32_16x16x32_f16 v[66:69], v[108:111], v[132:135], v[66:69]
	v_mfma_f32_16x16x32_f16 v[62:65], v[116:119], v[132:135], v[62:65]
	global_load_lds_dwordx4 v84, s[20:21]
	v_mfma_f32_16x16x32_f16 v[50:53], v[104:107], v[136:139], v[50:53]
	v_mfma_f32_16x16x32_f16 v[46:49], v[112:115], v[136:139], v[46:49]
	s_add_i32 s7, s7, 1
	s_cmp_lg_u32 s7, 16
	v_mfma_f32_16x16x32_f16 v[34:37], v[104:107], v[144:147], v[34:37]
	s_cselect_b32 s7, s7, 0
	v_mfma_f32_16x16x32_f16 v[30:33], v[112:115], v[144:147], v[30:33]
	s_add_i32 s11, s11, -1
	v_mfma_f32_16x16x32_f16 v[50:53], v[108:111], v[140:143], v[50:53]
	s_mov_b32 s15, s13
	v_mfma_f32_16x16x32_f16 v[46:49], v[116:119], v[140:143], v[46:49]
	s_mov_b32 s13, s14
	v_mfma_f32_16x16x32_f16 v[34:37], v[108:111], v[148:151], v[34:37]
	s_mov_b32 s14, s16
	v_mfma_f32_16x16x32_f16 v[30:33], v[116:119], v[148:151], v[30:33]
	s_cmp_lg_u32 s11, 0
	s_setprio 0
	s_barrier
	s_cbranch_scc1 .LBB2_3
	v_lshl_add_u32 v0, s0, 7, v86
	v_or_b32_e32 v88, s10, v1
	v_ashrrev_i32_e32 v1, 31, v0
	v_lshlrev_b64 v[82:83], 12, v[0:1]
	v_or_b32_e32 v88, s1, v88
	v_lshl_add_u64 v[82:83], s[8:9], 0, v[82:83]
	v_lshlrev_b32_e32 v88, 2, v88
	v_mov_b32_e32 v89, 0
	v_or_b32_e32 v84, 16, v0
	v_lshl_add_u64 v[82:83], v[82:83], 0, v[88:89]
	v_pk_add_f32 v[20:21], v[16:17], v[20:21]
	v_pk_add_f32 v[18:19], v[14:15], v[18:19]
	v_ashrrev_i32_e32 v85, 31, v84
	global_store_dwordx4 v[82:83], v[18:21], off sc1
	v_lshlrev_b64 v[84:85], 12, v[84:85]
	v_lshl_add_u64 v[84:85], s[8:9], 0, v[84:85]
	v_pk_add_f32 v[20:21], v[12:13], v[72:73]
	v_pk_add_f32 v[18:19], v[10:11], v[70:71]
	global_store_dwordx4 v[82:83], v[18:21], off offset:64 sc1
	v_or_b32_e32 v86, 32, v0
	v_lshl_add_u64 v[84:85], v[84:85], 0, v[88:89]
	v_pk_add_f32 v[20:21], v[8:9], v[80:81]
	v_pk_add_f32 v[18:19], v[6:7], v[78:79]
	global_store_dwordx4 v[82:83], v[18:21], off offset:512 sc1
	v_ashrrev_i32_e32 v87, 31, v86
	v_lshlrev_b64 v[86:87], 12, v[86:87]
	v_pk_add_f32 v[20:21], v[4:5], v[76:77]
	v_pk_add_f32 v[18:19], v[2:3], v[74:75]
	global_store_dwordx4 v[82:83], v[18:21], off offset:576 sc1
	v_lshl_add_u64 v[86:87], s[8:9], 0, v[86:87]
	v_or_b32_e32 v0, 48, v0
	v_pk_add_f32 v[20:21], v[16:17], v[60:61]
	v_pk_add_f32 v[18:19], v[14:15], v[58:59]
	global_store_dwordx4 v[84:85], v[18:21], off sc1
	v_ashrrev_i32_e32 v1, 31, v0
	v_lshl_add_u64 v[86:87], v[86:87], 0, v[88:89]
	v_pk_add_f32 v[20:21], v[12:13], v[56:57]
	v_pk_add_f32 v[18:19], v[10:11], v[54:55]
	global_store_dwordx4 v[84:85], v[18:21], off offset:64 sc1
	v_lshlrev_b64 v[0:1], 12, v[0:1]
	v_lshl_add_u64 v[0:1], s[8:9], 0, v[0:1]
	v_pk_add_f32 v[20:21], v[8:9], v[68:69]
	v_pk_add_f32 v[18:19], v[6:7], v[66:67]
	global_store_dwordx4 v[84:85], v[18:21], off offset:512 sc1
	v_lshl_add_u64 v[0:1], v[0:1], 0, v[88:89]
	s_cmpk_gt_u32 s12, 0xff
	v_pk_add_f32 v[20:21], v[4:5], v[64:65]
	v_pk_add_f32 v[18:19], v[2:3], v[62:63]
	global_store_dwordx4 v[84:85], v[18:21], off offset:576 sc1
	s_nop 1
	v_pk_add_f32 v[20:21], v[16:17], v[44:45]
	v_pk_add_f32 v[18:19], v[14:15], v[42:43]
	global_store_dwordx4 v[86:87], v[18:21], off sc1
	v_pk_add_f32 v[16:17], v[16:17], v[28:29]
	v_pk_add_f32 v[14:15], v[14:15], v[26:27]
	v_pk_add_f32 v[20:21], v[12:13], v[40:41]
	v_pk_add_f32 v[18:19], v[10:11], v[38:39]
	global_store_dwordx4 v[86:87], v[18:21], off offset:64 sc1
	v_pk_add_f32 v[12:13], v[12:13], v[24:25]
	v_pk_add_f32 v[10:11], v[10:11], v[22:23]
	v_pk_add_f32 v[20:21], v[8:9], v[52:53]
	v_pk_add_f32 v[18:19], v[6:7], v[50:51]
	global_store_dwordx4 v[86:87], v[18:21], off offset:512 sc1
	v_pk_add_f32 v[8:9], v[8:9], v[36:37]
	v_pk_add_f32 v[6:7], v[6:7], v[34:35]
	v_pk_add_f32 v[20:21], v[4:5], v[48:49]
	v_pk_add_f32 v[18:19], v[2:3], v[46:47]
	v_pk_add_f32 v[4:5], v[4:5], v[32:33]
	v_pk_add_f32 v[2:3], v[2:3], v[30:31]
	global_store_dwordx4 v[86:87], v[18:21], off offset:576 sc1
	global_store_dwordx4 v[0:1], v[14:17], off sc1
	global_store_dwordx4 v[0:1], v[10:13], off offset:64 sc1
	global_store_dwordx4 v[0:1], v[6:9], off offset:512 sc1
	global_store_dwordx4 v[0:1], v[2:5], off offset:576 sc1
	s_waitcnt vmcnt(0)
	s_cbranch_scc1 .LBB2_6
	s_barrier
